# v11_hazfix
# speedup vs baseline: 1.0108x; 1.0108x over previous
.LBB1_53:
	ds_read_b128 v[164:167], v205 offset:43008
	ds_read_b128 v[168:171], v205 offset:43040
	ds_read_b128 v[172:175], v205 offset:43072
	ds_read_b128 v[176:179], v205 offset:43104
	ds_read_b128 v[180:183], v205 offset:43136
	ds_read_b128 v[184:187], v205 offset:43168
	ds_read_b128 v[188:191], v205 offset:43200
	ds_read_b128 v[192:195], v205 offset:43232
	s_waitcnt vmcnt(17) lgkmcnt(7)
	v_mfma_f32_32x32x16_f16 v[34:49], v[112:115], v[164:167], 0
	s_waitcnt vmcnt(0)
	v_mfma_f32_32x32x16_f16 v[18:33], v[116:119], v[164:167], v[2:17]
	s_waitcnt lgkmcnt(6)
	v_mfma_f32_32x32x16_f16 v[34:49], v[100:103], v[168:171], v[34:49]
	v_mfma_f32_32x32x16_f16 v[18:33], v[120:123], v[168:171], v[18:33]
	s_waitcnt lgkmcnt(5)
	v_mfma_f32_32x32x16_f16 v[34:49], v[104:107], v[172:175], v[34:49]
	v_mfma_f32_32x32x16_f16 v[18:33], v[124:127], v[172:175], v[18:33]
	s_waitcnt lgkmcnt(4)
	v_mfma_f32_32x32x16_f16 v[34:49], v[108:111], v[176:179], v[34:49]
	v_mfma_f32_32x32x16_f16 v[18:33], v[128:131], v[176:179], v[18:33]
	s_waitcnt lgkmcnt(3)
	v_mfma_f32_32x32x16_f16 v[34:49], v[132:135], v[180:183], v[34:49]
	v_mfma_f32_32x32x16_f16 v[18:33], v[148:151], v[180:183], v[18:33]
	s_waitcnt lgkmcnt(2)
	v_mfma_f32_32x32x16_f16 v[34:49], v[136:139], v[184:187], v[34:49]
	v_mfma_f32_32x32x16_f16 v[18:33], v[152:155], v[184:187], v[18:33]
	s_waitcnt lgkmcnt(1)
	v_mfma_f32_32x32x16_f16 v[34:49], v[140:143], v[188:191], v[34:49]
	v_mfma_f32_32x32x16_f16 v[18:33], v[156:159], v[188:191], v[18:33]
	s_waitcnt lgkmcnt(0)
	v_mfma_f32_32x32x16_f16 v[34:49], v[144:147], v[192:195], v[34:49]
	v_mfma_f32_32x32x16_f16 v[18:33], v[160:163], v[192:195], v[18:33]
	s_nop 10
	v_cvt_pk_f16_f32 v41, v40, v41
	v_cvt_pk_f16_f32 v40, v38, v39
	v_cvt_pk_f16_f32 v39, v36, v37
	v_cvt_pk_f16_f32 v38, v34, v35
	v_cvt_pk_f16_f32 v25, v24, v25
	v_cvt_pk_f16_f32 v24, v22, v23
	v_cvt_pk_f16_f32 v23, v20, v21
	v_cvt_pk_f16_f32 v22, v18, v19
	v_cvt_pk_f16_f32 v21, v48, v49
	v_cvt_pk_f16_f32 v20, v46, v47
	v_cvt_pk_f16_f32 v19, v44, v45
	v_cvt_pk_f16_f32 v18, v42, v43
	v_mfma_f32_32x32x16_f16 v[50:65], v[38:41], v[22:25], 0
	v_cvt_pk_f16_f32 v25, v32, v33
	v_cvt_pk_f16_f32 v24, v30, v31
	v_cvt_pk_f16_f32 v23, v28, v29
	v_cvt_pk_f16_f32 v22, v26, v27
	s_nop 1
	v_mfma_f32_32x32x16_f16 v[34:49], v[18:21], v[22:25], 0
	v_mfma_f32_32x32x16_f16 v[18:33], v[164:167], v[96:99], 0
	v_mfma_f32_32x32x16_f16 v[18:33], v[168:171], v[76:79], v[18:33]
	s_nop 2
	v_max3_f32 v250, v50, v51, v52
	v_max3_f32 v250, v250, v53, v54
	v_max3_f32 v250, v250, v55, v56
	v_max_f32_e32 v251, v61, v61
	v_max_f32_e32 v252, v60, v60
	v_max3_f32 v250, v250, v57, v58
	v_max_f32_e32 v251, v252, v251
	v_mfma_f32_32x32x16_f16 v[18:33], v[172:175], v[72:75], v[18:33]
	v_max3_f32 v251, v250, v59, v251
	v_cndmask_b32_e64 v250, v250, v251, s[0:1]
	v_mov_b32_e32 v251, v250
	s_nop 1
	v_permlane32_swap_b32_e32 v250, v251
	v_max_f32_e32 v251, v251, v251
	v_max_f32_e32 v250, v250, v250
	v_max_f32_e32 v46, v250, v251
	v_mfma_f32_32x32x16_f16 v[18:33], v[176:179], v[68:71], v[18:33]
	v_sub_f32_e32 v47, v50, v46
	v_exp_f32_e32 v50, v47
	v_sub_f32_e32 v47, v51, v46
	v_sub_f32_e32 v48, v52, v46
	v_exp_f32_e32 v51, v47
	v_exp_f32_e32 v52, v48
	v_sub_f32_e32 v48, v53, v46
	v_sub_f32_e32 v49, v55, v46
	v_mfma_f32_32x32x16_f16 v[18:33], v[180:183], v[92:95], v[18:33]
	v_sub_f32_e32 v53, v57, v46
	v_exp_f32_e32 v55, v49
	v_sub_f32_e32 v49, v56, v46
	v_exp_f32_e32 v56, v53
	v_sub_f32_e32 v53, v58, v46
	v_exp_f32_e32 v62, v48
	v_sub_f32_e32 v48, v54, v46
	v_exp_f32_e32 v57, v53
	v_mfma_f32_32x32x16_f16 v[18:33], v[184:187], v[84:87], v[18:33]
	v_sub_f32_e32 v53, v59, v46
	v_add_f32_e32 v47, 0, v50
	v_exp_f32_e32 v48, v48
	v_exp_f32_e32 v53, v53
	v_add_f32_e32 v47, v51, v47
	v_add_f32_e32 v47, v52, v47
	v_exp_f32_e32 v49, v49
	v_add_f32_e32 v47, v62, v47
	v_mfma_f32_32x32x16_f16 v[18:33], v[188:191], v[88:91], v[18:33]
	v_add_f32_e32 v47, v48, v47
	v_cndmask_b32_e64 v58, v53, 0, s[14:15]
	v_sub_f32_e32 v53, v60, v46
	v_sub_f32_e32 v46, v61, v46
	v_add_f32_e32 v47, v55, v47
	v_exp_f32_e32 v53, v53
	v_exp_f32_e32 v46, v46
	v_add_f32_e32 v47, v49, v47
	v_mfma_f32_32x32x16_f16 v[18:33], v[192:195], v[80:83], v[18:33]
	ds_read_b128 v[192:195], v240 offset:48720
	ds_read_b128 v[188:191], v240 offset:48752
	ds_read_b128 v[184:187], v240 offset:48784
	ds_read_b128 v[180:183], v240 offset:48816
	ds_read_b128 v[176:179], v240 offset:48848
	ds_read_b128 v[172:175], v240 offset:48880
	ds_read_b128 v[168:171], v240 offset:48912
	ds_read_b128 v[164:167], v240 offset:48944
	v_add_f32_e32 v47, v56, v47
	v_add_f32_e32 v47, v57, v47
	v_add_f32_e32 v47, v58, v47
	v_cndmask_b32_e64 v59, v53, 0, s[14:15]
	v_cndmask_b32_e64 v60, v46, 0, s[14:15]
	v_cvt_pk_f16_f32 v46, v50, v51
	v_max3_f32 v50, v34, v35, v36
	v_add_f32_e32 v47, v59, v47
	v_max3_f32 v50, v50, v37, v38
	v_add_f32_e32 v53, v60, v47
	v_cvt_pk_f16_f32 v47, v52, v62
	v_max3_f32 v50, v50, v39, v40
	v_max_f32_e32 v51, v45, v45
	v_max_f32_e32 v52, v44, v44
	v_max3_f32 v50, v50, v41, v42
	v_max_f32_e32 v51, v52, v51
	v_max3_f32 v51, v50, v43, v51
	v_cndmask_b32_e64 v50, v50, v51, s[0:1]
	v_mov_b32_e32 v51, v50
	s_nop 1
	v_permlane32_swap_b32_e32 v50, v51
	s_waitcnt lgkmcnt(7)
	v_mfma_f32_32x32x16_f16 v[2:17], v[116:119], v[192:195], v[2:17]
	v_max_f32_e32 v51, v51, v51
	v_max_f32_e32 v50, v50, v50
	v_max_f32_e32 v50, v50, v51
	v_sub_f32_e32 v34, v34, v50
	v_exp_f32_e32 v52, v34
	v_sub_f32_e32 v34, v35, v50
	v_sub_f32_e32 v35, v36, v50
	s_waitcnt lgkmcnt(6)
	v_mfma_f32_32x32x16_f16 v[2:17], v[120:123], v[188:191], v[2:17]
	v_cvt_pk_f16_f32 v49, v49, v56
	v_exp_f32_e32 v56, v35
	v_sub_f32_e32 v35, v37, v50
	v_cvt_pk_f16_f32 v64, v57, v58
	v_exp_f32_e32 v57, v35
	v_sub_f32_e32 v35, v38, v50
	v_exp_f32_e32 v58, v35
	s_waitcnt lgkmcnt(5)
	v_mfma_f32_32x32x16_f16 v[2:17], v[124:127], v[184:187], v[2:17]
	v_sub_f32_e32 v35, v39, v50
	v_cvt_pk_f16_f32 v65, v59, v60
	v_exp_f32_e32 v60, v35
	v_sub_f32_e32 v35, v40, v50
	v_cvt_pk_f16_f32 v48, v48, v55
	v_exp_f32_e32 v55, v34
	v_exp_f32_e32 v62, v35
	s_waitcnt lgkmcnt(4)
	v_mfma_f32_32x32x16_f16 v[2:17], v[128:131], v[180:183], v[2:17]
	v_sub_f32_e32 v35, v41, v50
	v_exp_f32_e32 v63, v35
	v_sub_f32_e32 v35, v42, v50
	v_exp_f32_e32 v59, v35
	v_sub_f32_e32 v35, v43, v50
	v_add_f32_e32 v34, 0, v52
	v_exp_f32_e32 v35, v35
	s_waitcnt lgkmcnt(3)
	v_mfma_f32_32x32x16_f16 v[2:17], v[148:151], v[176:179], v[2:17]
	v_add_f32_e32 v34, v55, v34
	v_add_f32_e32 v34, v56, v34
	v_add_f32_e32 v34, v57, v34
	v_add_f32_e32 v34, v58, v34
	v_cndmask_b32_e64 v61, v35, 0, s[14:15]
	v_sub_f32_e32 v35, v44, v50
	v_add_f32_e32 v34, v60, v34
	s_waitcnt lgkmcnt(2)
	v_mfma_f32_32x32x16_f16 v[2:17], v[152:155], v[172:175], v[2:17]
	v_exp_f32_e32 v35, v35
	v_sub_f32_e32 v36, v45, v50
	v_cvt_pk_f16_f32 v25, v24, v25
	v_cvt_pk_f16_f32 v24, v22, v23
	v_cvt_pk_f16_f32 v23, v20, v21
	v_cvt_pk_f16_f32 v22, v18, v19
	v_add_f32_e32 v34, v62, v34
	s_waitcnt lgkmcnt(1)
	v_mfma_f32_32x32x16_f16 v[2:17], v[156:159], v[168:171], v[2:17]
	v_exp_f32_e32 v36, v36
	v_add_f32_e32 v34, v63, v34
	v_add_f32_e32 v34, v59, v34
	v_add_f32_e32 v34, v61, v34
	v_cndmask_b32_e64 v211, v35, 0, s[14:15]
	v_add_f32_e32 v18, v211, v34
	s_waitcnt lgkmcnt(0)
	v_mfma_f32_32x32x16_f16 v[2:17], v[160:163], v[164:167], v[2:17]
	v_cndmask_b32_e64 v250, v36, 0, s[14:15]
	v_cvt_pk_f16_f32 v51, v32, v33
	v_mfma_f32_32x32x16_f16 v[32:47], v[22:25], v[46:49], 0
	v_cvt_pk_f16_f32 v50, v30, v31
	v_cvt_pk_f16_f32 v49, v28, v29
	v_cvt_pk_f16_f32 v48, v26, v27
	v_mov_b32_e32 v67, v66
	v_add_f32_e32 v251, v250, v18
	v_mov_b32_e32 v54, v53
	v_mov_b32_e32 v252, v251
	v_mfma_f32_32x32x16_f16 v[32:47], v[48:51], v[64:67], v[32:47]
	v_permlane32_swap_b32_e32 v53, v54
	v_permlane32_swap_b32_e32 v251, v252
	s_and_saveexec_b64 s[2:3], s[4:5]
	s_cbranch_execz .LBB1_55
	v_add_f32_e32 v18, v53, v54
	v_rcp_f32_e32 v18, v18
	s_nop 5
	v_mov_b32_e32 v20, v33
	v_mov_b32_e32 v21, v34
	v_mov_b32_e32 v26, v37
	v_fma_mixlo_f16 v19, v18, v32, 0
	v_pk_mul_f32 v[20:21], v[18:19], v[20:21] op_sel_hi:[0,1]
	v_mov_b32_e32 v27, v38
	v_cvt_pk_f16_f32 v21, v20, v21
	v_pk_mul_f32 v[26:27], v[18:19], v[26:27] op_sel_hi:[0,1]
	v_fma_mixlo_f16 v28, v18, v36, 0
	v_pack_b32_f16 v20, v19, v21
	v_cvt_pk_f16_f32 v19, v26, v27
	v_fma_mixlo_f16 v27, v18, v35, 0
	v_fma_mixlo_f16 v18, v18, v39, 0
	v_pack_b32_f16 v26, v28, v19
	v_alignbit_b32 v21, v27, v21, 16
	v_alignbit_b32 v27, v18, v19, 16
	ds_write2_b64 v247, v[20:21], v[26:27] offset1:2
